# P3 stores write-back plus non-temporal hint
# baseline (speedup 1.0000x reference)
; __device__ __forceinline__ float shx(float v, int o, int lane) { return __builtin_bit_cast(float, __builtin_amdgcn_ds_bpermute((lane ^ o) << 2, __builtin_bit_cast(int, v))); }
; __device__ __forceinline__ int fresh_lane() { int l; asm volatile("v_mbcnt_lo_u32_b32 %0, -1, 0\n\tv_mbcnt_hi_u32_b32 %0, -1, %0" : "=v"(l)); return l; }
; __device__ __forceinline__ void rows_rstd(const float* ssp, int row0, int fq, int ln, float (&rs)[8]) {
;     f32x4 a[8], b[8];
; #pragma unroll
;     for (int q = 0; q < 8; ++q) { const f32x4* p = (const f32x4*)(ssp + (size_t)(row0 + (q >> 2) * 128 + (q & 3) * 16) * 32 + 8 * fq); a[q] = p[0]; b[q] = p[1]; }
; #pragma unroll
;     for (int q = 0; q < 8; ++q) { float s = ((a[q].x + a[q].y) + (a[q].z + a[q].w)) + ((b[q].x + b[q].y) + (b[q].z + b[q].w));
;         s += shx(s, 16, ln); s += shx(s, 32, ln); rs[q] = rsqrtf(s * (1.0f / D) + RMS_EPS); }
; }
;     __device__ __forceinline__ void operator()(AccRef acc, const Unit& u, int wr, int wc, int, int) const {
;         const int ln_ = fresh_lane(), fr = ln_ & 15, fq = ln_ >> 4;
;         const int row0 = u.pm * 256 + wr * 64 + fr, col0 = u.pn * 256 + wc * 32 + 8 * fq;
;         const __amdgpu_buffer_rsrc_t rsrc = __builtin_amdgcn_make_buffer_rsrc((void*)O, 0, (int)((size_t)M * DINP * 2), 0x00020000);
;         float rs[8]; rows_rstd(ss, row0, fq, ln_, rs);
.LBB0_342:
	s_lshl_b32 s6, s6, 8
	v_mbcnt_lo_u32_b32 v178, -1, 0
	v_mbcnt_hi_u32_b32 v178, -1, v178
	s_add_i32 s6, s6, s38
	v_ashrrev_i32_e32 v130, 1, v178
	v_and_or_b32 v200, v178, 15, s6
	s_lshl_b32 s6, s7, 8
	v_and_b32_e32 v130, -8, v130
	s_or_b32 s6, s6, s39
	v_ashrrev_i32_e32 v131, 31, v130
	v_ashrrev_i32_e32 v201, 31, v200
	v_add_u32_e32 v209, s6, v130
	v_lshl_add_u64 v[130:131], v[130:131], 2, s[8:9]
	v_lshlrev_b64 v[132:133], 7, v[200:201]
	v_or_b32_e32 v134, 16, v200
	v_lshl_add_u64 v[132:133], v[130:131], 0, v[132:133]
	v_ashrrev_i32_e32 v135, 31, v134
	s_nop 0
	s_nop 0
	v_lshlrev_b64 v[134:135], 7, v[134:135]
	v_lshl_add_u64 v[134:135], v[130:131], 0, v[134:135]
	s_nop 0
	s_nop 0
	v_or_b32_e32 v134, 32, v200
	v_ashrrev_i32_e32 v135, 31, v134
	v_lshlrev_b64 v[134:135], 7, v[134:135]
	v_lshl_add_u64 v[134:135], v[130:131], 0, v[134:135]
	s_nop 0
	s_nop 0
	v_or_b32_e32 v134, 48, v200
	v_ashrrev_i32_e32 v135, 31, v134
	v_lshlrev_b64 v[134:135], 7, v[134:135]
	v_lshl_add_u64 v[130:131], v[130:131], 0, v[134:135]
	s_nop 0
	s_nop 0
	v_add_co_u32_e32 v134, vcc, s71, v132
	v_lshl_add_u64 v[130:131], v[132:133], 0, s[92:93]
	s_nop 0
	v_addc_co_u32_e32 v135, vcc, 0, v133, vcc
	v_add_co_u32_e32 v136, vcc, s72, v132
	s_mov_b64 s[6:7], 0x5000
	s_nop 0
	v_addc_co_u32_e32 v137, vcc, 0, v133, vcc
	s_nop 0
	s_nop 0
	v_lshl_add_u64 v[130:131], v[132:133], 0, s[94:95]
	s_nop 0
	s_nop 0
	v_lshl_add_u64 v[130:131], v[132:133], 0, s[6:7]
	s_nop 0
	s_nop 0
	s_mov_b64 s[6:7], 0x5800
	v_lshl_add_u64 v[130:131], v[132:133], 0, s[6:7]
	s_nop 0
	s_nop 0
	s_nop 0
	v_lshlrev_b32_e32 v178, 2, v178
	v_xor_b32_e32 v224, 64, v178
	v_xor_b32_e32 v201, 0x80, v178
	s_mov_b32 s6, 0x358637bd
	v_mov_b64_e32 v[206:207], s[6:7]
	s_mov_b32 s20, 0x3a000000
	s_mov_b32 s13, 0x800000
	s_nop 0
	v_mov_b32_e32 v178, v226
	v_mov_b32_e32 v179, v230
	v_mov_b32_e32 v230, v227
	v_mov_b32_e32 v180, v228
	v_mov_b32_e32 v181, v232
	v_mov_b32_e32 v232, v229
	v_pk_add_f32 v[178:179], v[178:179], v[230:231]
	v_pk_add_f32 v[180:181], v[180:181], v[232:233]
	v_mov_b32_e32 v182, v236
	v_pk_add_f32 v[178:179], v[178:179], v[180:181]
	v_mov_b32_e32 v180, v234
	v_mov_b32_e32 v181, v238
	v_mov_b32_e32 v238, v235
	v_mov_b32_e32 v183, v240
	v_mov_b32_e32 v240, v237
	v_pk_add_f32 v[180:181], v[180:181], v[238:239]
	v_pk_add_f32 v[182:183], v[182:183], v[240:241]
	s_nop 0
	v_pk_add_f32 v[180:181], v[180:181], v[182:183]
	v_mov_b32_e32 v183, v178
	v_mov_b32_e32 v182, v180
	v_mov_b32_e32 v178, v181
	v_pk_add_f32 v[178:179], v[182:183], v[178:179]
	ds_bpermute_b32 v181, v224, v179
	ds_bpermute_b32 v180, v224, v178
	s_waitcnt lgkmcnt(0)
	v_pk_add_f32 v[178:179], v[178:179], v[180:181]
	ds_bpermute_b32 v181, v201, v179
	ds_bpermute_b32 v180, v201, v178
	s_waitcnt lgkmcnt(0)
	v_pk_add_f32 v[178:179], v[178:179], v[180:181]
	s_nop 0
	v_pk_fma_f32 v[178:179], v[178:179], s[20:21], v[206:207] op_sel_hi:[1,0,0]
	s_nop 0
	v_mul_f32_e32 v180, 0x4b800000, v179
	v_cmp_gt_f32_e64 s[6:7], s13, v179
	v_cmp_gt_f32_e32 vcc, s13, v178
	s_nop 0
	v_cndmask_b32_e64 v179, v179, v180, s[6:7]
	v_rsq_f32_e32 v179, v179
	s_nop 0
	v_mul_f32_e32 v180, 0x45800000, v179
	v_cndmask_b32_e64 v204, v179, v180, s[6:7]
	v_mov_b32_e32 v204, v242
	v_mul_f32_e32 v179, 0x4b800000, v178
	v_cndmask_b32_e32 v178, v178, v179, vcc
	v_rsq_f32_e32 v178, v178
	v_pk_mul_f32 v[128:129], v[128:129], v[204:205] op_sel_hi:[1,0]
	v_pk_mul_f32 v[126:127], v[126:127], v[204:205] op_sel_hi:[1,0]
	v_pk_mul_f32 v[120:121], v[120:121], v[204:205] op_sel_hi:[1,0]
	v_mul_f32_e32 v179, 0x45800000, v178
	v_cndmask_b32_e32 v202, v178, v179, vcc
	v_mov_b32_e32 v202, v243
	v_mov_b32_e32 v178, v170
	v_mov_b32_e32 v179, v174
	v_mov_b32_e32 v174, v171
	v_pk_add_f32 v[170:171], v[178:179], v[174:175]
	v_mov_b32_e32 v174, v172
	v_mov_b32_e32 v175, v176
	v_mov_b32_e32 v176, v173
	v_pk_add_f32 v[172:173], v[174:175], v[176:177]
	v_pk_mul_f32 v[118:119], v[118:119], v[204:205] op_sel_hi:[1,0]
	v_pk_add_f32 v[170:171], v[170:171], v[172:173]
	v_mov_b32_e32 v172, v166
	v_mov_b32_e32 v173, v162
	v_mov_b32_e32 v162, v167
	v_mov_b32_e32 v166, v168
	v_mov_b32_e32 v167, v164
	v_mov_b32_e32 v164, v169
	v_pk_add_f32 v[162:163], v[172:173], v[162:163]
	v_pk_add_f32 v[164:165], v[166:167], v[164:165]
	v_mov_b32_e32 v166, v158
	v_pk_add_f32 v[162:163], v[162:163], v[164:165]
	v_mov_b32_e32 v165, v170
	v_mov_b32_e32 v164, v162
	v_mov_b32_e32 v170, v163
	v_pk_add_f32 v[162:163], v[164:165], v[170:171]
	ds_bpermute_b32 v165, v224, v163
	ds_bpermute_b32 v164, v224, v162
	v_mov_b32_e32 v167, v154
	v_mov_b32_e32 v154, v159
	v_mov_b32_e32 v158, v160
	v_mov_b32_e32 v159, v156
	v_mov_b32_e32 v156, v161
	v_pk_add_f32 v[154:155], v[166:167], v[154:155]
	v_pk_add_f32 v[156:157], v[158:159], v[156:157]
	s_waitcnt lgkmcnt(0)
	v_pk_add_f32 v[162:163], v[162:163], v[164:165]
	v_pk_add_f32 v[154:155], v[154:155], v[156:157]
	v_mov_b32_e32 v156, v150
	v_mov_b32_e32 v157, v146
	v_mov_b32_e32 v146, v151
	v_mov_b32_e32 v150, v152
	v_mov_b32_e32 v151, v148
	v_mov_b32_e32 v148, v153
	v_pk_add_f32 v[146:147], v[156:157], v[146:147]
	v_pk_add_f32 v[148:149], v[150:151], v[148:149]
	ds_bpermute_b32 v165, v201, v163
	v_pk_add_f32 v[146:147], v[146:147], v[148:149]
	v_mov_b32_e32 v149, v154
	v_mov_b32_e32 v148, v146
	v_mov_b32_e32 v154, v147
	ds_bpermute_b32 v164, v201, v162
	v_pk_add_f32 v[146:147], v[148:149], v[154:155]
	ds_bpermute_b32 v149, v224, v147
	ds_bpermute_b32 v148, v224, v146
	v_mov_b32_e32 v150, v142
	v_mov_b32_e32 v151, v138
	v_mov_b32_e32 v138, v143
	v_mov_b32_e32 v142, v144
	v_mov_b32_e32 v143, v140
	v_mov_b32_e32 v140, v145
	v_pk_add_f32 v[138:139], v[150:151], v[138:139]
	v_pk_add_f32 v[140:141], v[142:143], v[140:141]
	s_waitcnt lgkmcnt(2)
; __device__ __forceinline__ unsigned cvt_pk_bf16(float lo, float hi) { unsigned r; asm volatile("v_cvt_pk_bf16_f32 %0, %1, %2" : "=v"(r) : "v"(lo), "v"(hi)); return r; }
; __device__ __forceinline__ float shx(float v, int o, int lane) { return __builtin_bit_cast(float, __builtin_amdgcn_ds_bpermute((lane ^ o) << 2, __builtin_bit_cast(int, v))); }
; __device__ __forceinline__ void store16_wt(__amdgpu_buffer_rsrc_t rsrc, unsigned byte_off, v4u v) { __builtin_amdgcn_raw_buffer_store_b128(v, rsrc, byte_off, 0, 16); }
; __device__ __forceinline__ void rows_rstd(const float* ssp, int row0, int fq, int ln, float (&rs)[8]) {
;     ...
;     for (int q = 0; q < 8; ++q) { float s = ((a[q].x + a[q].y) + (a[q].z + a[q].w)) + ((b[q].x + b[q].y) + (b[q].z + b[q].w));
;         s += shx(s, 16, ln); s += shx(s, 32, ln); rs[q] = rsqrtf(s * (1.0f / D) + RMS_EPS); }
;     __device__ __forceinline__ void operator()(AccRef acc, const Unit& u, int wr, int wc, int, int) const {
;     ...
;         for (int ai = 0; ai < 2; ++ai)
; #pragma unroll
;             for (int m = 0; m < 4; ++m) {
;                 const int row = row0 + ai * 128 + m * 16;
;                 const float r = rs[ai * 4 + m];
; #pragma unroll
;                 for (int bj = 0; bj < 2; ++bj) {
;                     const f32x4 v0 = acc[ai][bj][m][0] * r, v1 = acc[ai][bj][m][1] * r;
;                     v4u w; w.x = cvt_pk_bf16(v0[0], v0[1]); w.y = cvt_pk_bf16(v0[2], v0[3]); w.z = cvt_pk_bf16(v1[0], v1[1]); w.w = cvt_pk_bf16(v1[2], v1[3]);
;                     store16_wt(rsrc, (unsigned)(((size_t)row * DINP + col0 + bj * 128) * 2), w);
;                 }
	v_pk_add_f32 v[162:163], v[162:163], v[164:165]
	v_pk_add_f32 v[138:139], v[138:139], v[140:141]
	v_mov_b32_e32 v140, v134
	v_mov_b32_e32 v141, v130
	v_mov_b32_e32 v130, v135
	v_mov_b32_e32 v134, v136
	v_mov_b32_e32 v135, v132
	v_mov_b32_e32 v132, v137
	v_pk_add_f32 v[130:131], v[140:141], v[130:131]
	v_pk_add_f32 v[132:133], v[134:135], v[132:133]
	v_pk_fma_f32 v[162:163], v[162:163], s[20:21], v[206:207] op_sel_hi:[1,0,0]
	v_pk_add_f32 v[130:131], v[130:131], v[132:133]
	s_waitcnt lgkmcnt(0)
	v_pk_add_f32 v[146:147], v[146:147], v[148:149]
	v_mov_b32_e32 v132, v130
	v_mov_b32_e32 v133, v138
	v_mov_b32_e32 v138, v131
	v_mul_f32_e32 v164, 0x4b800000, v163
	v_cmp_gt_f32_e64 s[6:7], s13, v163
	ds_bpermute_b32 v149, v201, v147
	ds_bpermute_b32 v148, v201, v146
	v_pk_add_f32 v[130:131], v[132:133], v[138:139]
	v_cndmask_b32_e64 v163, v163, v164, s[6:7]
	ds_bpermute_b32 v133, v224, v131
	ds_bpermute_b32 v132, v224, v130
	v_rsq_f32_e32 v163, v163
	s_waitcnt lgkmcnt(2)
	v_pk_add_f32 v[146:147], v[146:147], v[148:149]
	v_cmp_gt_f32_e32 vcc, s13, v162
	v_pk_fma_f32 v[146:147], v[146:147], s[20:21], v[206:207] op_sel_hi:[1,0,0]
	v_mul_f32_e32 v164, 0x45800000, v163
	s_waitcnt lgkmcnt(0)
	v_pk_add_f32 v[130:131], v[130:131], v[132:133]
	v_cndmask_b32_e64 v164, v163, v164, s[6:7]
	v_mov_b32_e32 v164, v244
	v_mul_f32_e32 v163, 0x4b800000, v162
	v_mul_f32_e32 v148, 0x4b800000, v147
	v_cmp_gt_f32_e64 s[6:7], s13, v147
	ds_bpermute_b32 v133, v201, v131
	ds_bpermute_b32 v132, v201, v130
	v_cndmask_b32_e32 v162, v162, v163, vcc
	v_cndmask_b32_e64 v147, v147, v148, s[6:7]
	v_rsq_f32_e32 v162, v162
	v_rsq_f32_e32 v147, v147
	s_waitcnt lgkmcnt(0)
	v_pk_add_f32 v[130:131], v[130:131], v[132:133]
	v_pk_mul_f32 v[134:135], v[124:125], v[204:205] op_sel_hi:[1,0]
	v_mul_f32_e32 v163, 0x45800000, v162
	v_mul_f32_e32 v148, 0x45800000, v147
	v_pk_fma_f32 v[130:131], v[130:131], s[20:21], v[206:207] op_sel_hi:[1,0,0]
	v_cndmask_b32_e32 v162, v162, v163, vcc
	v_mov_b32_e32 v162, v245
	v_cmp_gt_f32_e32 vcc, s13, v146
	v_cndmask_b32_e64 v148, v147, v148, s[6:7]
	v_mov_b32_e32 v148, v246
	v_mul_f32_e32 v147, 0x4b800000, v146
	v_mul_f32_e32 v132, 0x4b800000, v131
	v_cmp_gt_f32_e64 s[6:7], s13, v131
	v_cndmask_b32_e32 v146, v146, v147, vcc
	v_rsq_f32_e32 v146, v146
	v_cndmask_b32_e64 v131, v131, v132, s[6:7]
	v_rsq_f32_e32 v131, v131
	v_readlane_b32 s20, v254, 19
	v_mul_f32_e32 v147, 0x45800000, v146
	v_cndmask_b32_e32 v146, v146, v147, vcc
	v_mov_b32_e32 v146, v247
	v_mul_f32_e32 v132, 0x45800000, v131
	v_cmp_gt_f32_e32 vcc, s13, v130
	v_cndmask_b32_e64 v132, v131, v132, s[6:7]
	v_mov_b32_e32 v132, v248
	v_mul_f32_e32 v131, 0x4b800000, v130
	v_cndmask_b32_e32 v130, v130, v131, vcc
	v_rsq_f32_e32 v130, v130
	s_movk_i32 s6, 0x3c00
	v_pk_mul_f32 v[124:125], v[122:123], v[204:205] op_sel_hi:[1,0]
	v_cvt_pk_bf16_f32 v122, v126, v127
	v_mul_f32_e32 v131, 0x45800000, v130
	v_cndmask_b32_e32 v130, v130, v131, vcc
	v_mov_b32_e32 v130, v249
	v_mul_lo_u32 v131, v200, s6
	v_add_lshl_u32 v131, v209, v131, 1
	v_cvt_pk_bf16_f32 v123, v128, v129
	v_readlane_b32 s21, v254, 20
	v_readlane_b32 s22, v254, 21
	v_readlane_b32 s23, v254, 22
	v_cvt_pk_bf16_f32 v124, v124, v125
	v_cvt_pk_bf16_f32 v125, v134, v135
	v_pk_mul_f32 v[104:105], v[104:105], v[202:203] op_sel_hi:[1,0]
	v_pk_mul_f32 v[102:103], v[102:103], v[202:203] op_sel_hi:[1,0]
	v_pk_mul_f32 v[88:89], v[88:89], v[164:165] op_sel_hi:[1,0]
	s_nop 1
	buffer_store_dwordx4 v[122:125], v131, s[20:23], 0 offen nt
	v_pk_mul_f32 v[86:87], v[86:87], v[164:165] op_sel_hi:[1,0]
	v_pk_mul_f32 v[72:73], v[72:73], v[162:163] op_sel_hi:[1,0]
	v_pk_mul_f32 v[122:123], v[112:113], v[204:205] op_sel_hi:[1,0]
	v_pk_mul_f32 v[112:113], v[110:111], v[204:205] op_sel_hi:[1,0]
	v_cvt_pk_bf16_f32 v110, v118, v119
	v_cvt_pk_bf16_f32 v111, v120, v121
	v_add_u32_e32 v118, 0x78000, v131
	v_cvt_pk_bf16_f32 v112, v112, v113
	v_cvt_pk_bf16_f32 v113, v122, v123
	buffer_store_dwordx4 v[110:113], v131, s[20:23], 0 offen offset:256 nt
	v_pk_mul_f32 v[70:71], v[70:71], v[162:163] op_sel_hi:[1,0]
	v_pk_mul_f32 v[64:65], v[64:65], v[148:149] op_sel_hi:[1,0]
	v_pk_mul_f32 v[110:111], v[116:117], v[202:203] op_sel_hi:[1,0]
	v_pk_mul_f32 v[112:113], v[114:115], v[202:203] op_sel_hi:[1,0]
	v_pk_mul_f32 v[114:115], v[108:109], v[202:203] op_sel_hi:[1,0]
	v_pk_mul_f32 v[108:109], v[106:107], v[202:203] op_sel_hi:[1,0]
	v_cvt_pk_bf16_f32 v106, v112, v113
	v_cvt_pk_bf16_f32 v107, v110, v111
	v_pk_mul_f32 v[62:63], v[62:63], v[148:149] op_sel_hi:[1,0]
	v_cvt_pk_bf16_f32 v108, v108, v109
	v_cvt_pk_bf16_f32 v109, v114, v115
	buffer_store_dwordx4 v[106:109], v118, s[20:23], 0 offen nt
	v_pk_mul_f32 v[56:57], v[56:57], v[148:149] op_sel_hi:[1,0]
	v_pk_mul_f32 v[54:55], v[54:55], v[148:149] op_sel_hi:[1,0]
	v_pk_mul_f32 v[106:107], v[96:97], v[202:203] op_sel_hi:[1,0]
	v_pk_mul_f32 v[96:97], v[94:95], v[202:203] op_sel_hi:[1,0]
	v_cvt_pk_bf16_f32 v94, v102, v103
	v_cvt_pk_bf16_f32 v95, v104, v105
	v_add_u32_e32 v102, 0xf0000, v131
	v_cvt_pk_bf16_f32 v96, v96, v97
	v_cvt_pk_bf16_f32 v97, v106, v107
	buffer_store_dwordx4 v[94:97], v118, s[20:23], 0 offen offset:256 nt
	v_pk_mul_f32 v[40:41], v[40:41], v[146:147] op_sel_hi:[1,0]
; __device__ __forceinline__ unsigned cvt_pk_bf16(float lo, float hi) { unsigned r; asm volatile("v_cvt_pk_bf16_f32 %0, %1, %2" : "=v"(r) : "v"(lo), "v"(hi)); return r; }
; __device__ __forceinline__ void store16_wt(__amdgpu_buffer_rsrc_t rsrc, unsigned byte_off, v4u v) { __builtin_amdgcn_raw_buffer_store_b128(v, rsrc, byte_off, 0, 16); }
;     __device__ __forceinline__ void operator()(AccRef acc, const Unit& u, int wr, int wc, int, int) const {
;     ...
;         for (int ai = 0; ai < 2; ++ai)
; #pragma unroll
;             for (int m = 0; m < 4; ++m) {
;                 const int row = row0 + ai * 128 + m * 16;
;                 const float r = rs[ai * 4 + m];
; #pragma unroll
;                 for (int bj = 0; bj < 2; ++bj) {
;                     const f32x4 v0 = acc[ai][bj][m][0] * r, v1 = acc[ai][bj][m][1] * r;
;                     v4u w; w.x = cvt_pk_bf16(v0[0], v0[1]); w.y = cvt_pk_bf16(v0[2], v0[3]); w.z = cvt_pk_bf16(v1[0], v1[1]); w.w = cvt_pk_bf16(v1[2], v1[3]);
;                     store16_wt(rsrc, (unsigned)(((size_t)row * DINP + col0 + bj * 128) * 2), w);
;                 }
	v_pk_mul_f32 v[38:39], v[38:39], v[146:147] op_sel_hi:[1,0]
	v_pk_mul_f32 v[94:95], v[100:101], v[164:165] op_sel_hi:[1,0]
	v_pk_mul_f32 v[96:97], v[98:99], v[164:165] op_sel_hi:[1,0]
	v_pk_mul_f32 v[98:99], v[92:93], v[164:165] op_sel_hi:[1,0]
	v_pk_mul_f32 v[92:93], v[90:91], v[164:165] op_sel_hi:[1,0]
	v_cvt_pk_bf16_f32 v90, v96, v97
	v_cvt_pk_bf16_f32 v91, v94, v95
	v_pk_mul_f32 v[24:25], v[24:25], v[132:133] op_sel_hi:[1,0]
	v_cvt_pk_bf16_f32 v92, v92, v93
	v_cvt_pk_bf16_f32 v93, v98, v99
	buffer_store_dwordx4 v[90:93], v102, s[20:23], 0 offen nt
	v_pk_mul_f32 v[22:23], v[22:23], v[132:133] op_sel_hi:[1,0]
	s_mov_b64 s[6:7], -1
	v_pk_mul_f32 v[90:91], v[80:81], v[164:165] op_sel_hi:[1,0]
	v_pk_mul_f32 v[80:81], v[78:79], v[164:165] op_sel_hi:[1,0]
	v_cvt_pk_bf16_f32 v78, v86, v87
	v_cvt_pk_bf16_f32 v79, v88, v89
	v_add_u32_e32 v86, 0x168000, v131
	v_cvt_pk_bf16_f32 v80, v80, v81
	v_cvt_pk_bf16_f32 v81, v90, v91
	buffer_store_dwordx4 v[78:81], v102, s[20:23], 0 offen offset:256 nt
	s_andn2_b64 vcc, exec, s[4:5]
	v_pk_mul_f32 v[6:7], v[6:7], v[130:131] op_sel_hi:[1,0]
	v_pk_mul_f32 v[78:79], v[84:85], v[162:163] op_sel_hi:[1,0]
	v_pk_mul_f32 v[80:81], v[82:83], v[162:163] op_sel_hi:[1,0]
	v_pk_mul_f32 v[82:83], v[76:77], v[162:163] op_sel_hi:[1,0]
	v_pk_mul_f32 v[76:77], v[74:75], v[162:163] op_sel_hi:[1,0]
	v_cvt_pk_bf16_f32 v74, v80, v81
	v_cvt_pk_bf16_f32 v75, v78, v79
	v_pk_mul_f32 v[4:5], v[4:5], v[130:131] op_sel_hi:[1,0]
	v_cvt_pk_bf16_f32 v76, v76, v77
	v_cvt_pk_bf16_f32 v77, v82, v83
	buffer_store_dwordx4 v[74:77], v86, s[20:23], 0 offen nt
	s_nop 1
	v_pk_mul_f32 v[74:75], v[68:69], v[162:163] op_sel_hi:[1,0]
	v_pk_mul_f32 v[68:69], v[66:67], v[162:163] op_sel_hi:[1,0]
	v_cvt_pk_bf16_f32 v66, v70, v71
	v_cvt_pk_bf16_f32 v67, v72, v73
	s_nop 0
	v_cvt_pk_bf16_f32 v68, v68, v69
	v_cvt_pk_bf16_f32 v69, v74, v75
	buffer_store_dwordx4 v[66:69], v86, s[20:23], 0 offen offset:256 nt
	s_nop 1
	v_add_u32_e32 v68, 0x3c0000, v131
	v_pk_mul_f32 v[66:67], v[60:61], v[148:149] op_sel_hi:[1,0]
	v_pk_mul_f32 v[60:61], v[58:59], v[148:149] op_sel_hi:[1,0]
	v_cvt_pk_bf16_f32 v58, v62, v63
	v_cvt_pk_bf16_f32 v59, v64, v65
	s_nop 0
	v_cvt_pk_bf16_f32 v60, v60, v61
	v_cvt_pk_bf16_f32 v61, v66, v67
	buffer_store_dwordx4 v[58:61], v68, s[20:23], 0 offen nt
	s_nop 1
	v_pk_mul_f32 v[58:59], v[48:49], v[148:149] op_sel_hi:[1,0]
	v_pk_mul_f32 v[48:49], v[46:47], v[148:149] op_sel_hi:[1,0]
	v_cvt_pk_bf16_f32 v46, v54, v55
	v_cvt_pk_bf16_f32 v47, v56, v57
	v_add_u32_e32 v54, 0x438000, v131
	v_cvt_pk_bf16_f32 v48, v48, v49
	v_cvt_pk_bf16_f32 v49, v58, v59
	buffer_store_dwordx4 v[46:49], v68, s[20:23], 0 offen offset:256 nt
	s_nop 1
	v_pk_mul_f32 v[46:47], v[52:53], v[146:147] op_sel_hi:[1,0]
	v_pk_mul_f32 v[48:49], v[50:51], v[146:147] op_sel_hi:[1,0]
	v_pk_mul_f32 v[50:51], v[44:45], v[146:147] op_sel_hi:[1,0]
	v_pk_mul_f32 v[44:45], v[42:43], v[146:147] op_sel_hi:[1,0]
	v_cvt_pk_bf16_f32 v42, v48, v49
	v_cvt_pk_bf16_f32 v43, v46, v47
	s_nop 0
	v_cvt_pk_bf16_f32 v44, v44, v45
	v_cvt_pk_bf16_f32 v45, v50, v51
	buffer_store_dwordx4 v[42:45], v54, s[20:23], 0 offen nt
	s_nop 1
	v_pk_mul_f32 v[42:43], v[32:33], v[146:147] op_sel_hi:[1,0]
	v_pk_mul_f32 v[32:33], v[30:31], v[146:147] op_sel_hi:[1,0]
	v_cvt_pk_bf16_f32 v30, v38, v39
	v_cvt_pk_bf16_f32 v31, v40, v41
	v_add_u32_e32 v38, 0x4b0000, v131
	v_cvt_pk_bf16_f32 v32, v32, v33
	v_cvt_pk_bf16_f32 v33, v42, v43
	buffer_store_dwordx4 v[30:33], v54, s[20:23], 0 offen offset:256 nt
	s_nop 1
	v_pk_mul_f32 v[30:31], v[36:37], v[132:133] op_sel_hi:[1,0]
	v_pk_mul_f32 v[32:33], v[34:35], v[132:133] op_sel_hi:[1,0]
	v_pk_mul_f32 v[34:35], v[28:29], v[132:133] op_sel_hi:[1,0]
	v_pk_mul_f32 v[28:29], v[26:27], v[132:133] op_sel_hi:[1,0]
	v_cvt_pk_bf16_f32 v26, v32, v33
	v_cvt_pk_bf16_f32 v27, v30, v31
	s_nop 0
	v_cvt_pk_bf16_f32 v28, v28, v29
	v_cvt_pk_bf16_f32 v29, v34, v35
	buffer_store_dwordx4 v[26:29], v38, s[20:23], 0 offen nt
	s_nop 1
	v_pk_mul_f32 v[26:27], v[16:17], v[132:133] op_sel_hi:[1,0]
	v_pk_mul_f32 v[16:17], v[14:15], v[132:133] op_sel_hi:[1,0]
	v_cvt_pk_bf16_f32 v14, v22, v23
	v_cvt_pk_bf16_f32 v15, v24, v25
	v_add_u32_e32 v22, 0x528000, v131
	v_cvt_pk_bf16_f32 v16, v16, v17
	v_cvt_pk_bf16_f32 v17, v26, v27
	buffer_store_dwordx4 v[14:17], v38, s[20:23], 0 offen offset:256 nt
	s_nop 1
	v_pk_mul_f32 v[14:15], v[20:21], v[130:131] op_sel_hi:[1,0]
	v_pk_mul_f32 v[16:17], v[18:19], v[130:131] op_sel_hi:[1,0]
	v_pk_mul_f32 v[18:19], v[12:13], v[130:131] op_sel_hi:[1,0]
	v_pk_mul_f32 v[12:13], v[10:11], v[130:131] op_sel_hi:[1,0]
	v_cvt_pk_bf16_f32 v10, v16, v17
	v_cvt_pk_bf16_f32 v11, v14, v15
	s_nop 0
	v_cvt_pk_bf16_f32 v12, v12, v13
	v_cvt_pk_bf16_f32 v13, v18, v19
	buffer_store_dwordx4 v[10:13], v22, s[20:23], 0 offen nt
	s_nop 1
	v_pk_mul_f32 v[10:11], v[2:3], v[130:131] op_sel_hi:[1,0]
	v_pk_mul_f32 v[2:3], v[0:1], v[130:131] op_sel_hi:[1,0]
	v_cvt_pk_bf16_f32 v0, v4, v5
	v_cvt_pk_bf16_f32 v1, v6, v7
	s_nop 0
	v_cvt_pk_bf16_f32 v2, v2, v3
	v_cvt_pk_bf16_f32 v3, v10, v11
	buffer_store_dwordx4 v[0:3], v22, s[20:23], 0 offen offset:256 nt
	s_cbranch_vccnz .LBB0_335
	s_andn2_b64 vcc, exec, s[0:1]
	s_cbranch_vccnz .LBB0_334
	s_barrier
	s_branch .LBB0_334
